# GU K-loop first trip peeled (SrcC=0, accumulator zero block removed), stage loads retired at epilogue end, first-trip waits relaxed
# baseline (speedup 1.0000x reference)
.LBB0_746:
	s_andn2_b64 vcc, exec, s[22:23]
	s_cbranch_vccnz .LBB0_761
	s_add_u32 s69, s40, 0x100
	s_addc_u32 s70, s41, 0
	s_add_u32 s8, s42, 0x80
	v_mov_b32_e32 v37, v1
	v_mov_b32_e32 v207, v1
	v_mov_b32_e32 v35, v1
	v_mov_b64_e32 v[208:209], v[0:1]
	s_addc_u32 s9, s43, 0
	s_mov_b32 s71, 0
	s_cmp_eq_u32 s64, s71
	s_cselect_b64 s[4:5], -1, 0
	s_add_u32 s72, s8, 0x80
	s_addc_u32 s73, s9, 0
	s_and_b64 s[40:41], s[4:5], exec
	s_cselect_b32 s43, s31, s70
	s_cselect_b32 s42, s30, s69
	s_add_i32 s76, 0, 0x10000
	s_and_b64 s[40:41], s[4:5], exec
	v_add_u32_e32 v0, s76, v244
	s_cselect_b32 s41, s37, s73
	s_cselect_b32 s40, s36, s72
	s_add_i32 s72, 0, 0x14000
	ds_read_b128 v[150:153], v0
	ds_read_b128 v[154:157], v0 offset:1024
	ds_read_b128 v[158:161], v0 offset:2048
	ds_read_b128 v[162:165], v0 offset:3072
	v_add_u32_e32 v0, s72, v244
	ds_read_b128 v[134:137], v0
	ds_read_b128 v[138:141], v0 offset:1024
	ds_read_b128 v[142:145], v0 offset:2048
	ds_read_b128 v[146:149], v0 offset:3072
	v_lshl_add_u64 v[210:211], s[8:9], 0, v[36:37]
	s_add_i32 m0, s48, 0xc000
	ds_read_b128 v[166:169], v247
	ds_read_b128 v[170:173], v247 offset:1024
	ds_read_b128 v[174:177], v247 offset:2048
	ds_read_b128 v[178:181], v247 offset:3072
	ds_read_b128 v[182:185], v247 offset:4096
	ds_read_b128 v[186:189], v247 offset:5120
	ds_read_b128 v[190:193], v247 offset:6144
	ds_read_b128 v[194:197], v247 offset:7168
	global_load_lds_dwordx4 v[210:211], off
	v_lshl_add_u64 v[210:211], s[8:9], 0, v[206:207]
	s_add_i32 m0, s48, 0xe000
	s_nop 0
	global_load_lds_dwordx4 v[210:211], off
	s_waitcnt lgkmcnt(0)
	s_barrier
	s_setprio 1
	s_waitcnt lgkmcnt(0)
	v_mfma_f32_16x16x32_bf16 v[130:133], v[150:153], v[166:169], 0
	v_mfma_f32_16x16x32_bf16 v[122:125], v[158:161], v[166:169], 0
	v_mfma_f32_16x16x32_bf16 v[114:117], v[150:153], v[174:177], 0
	v_mfma_f32_16x16x32_bf16 v[106:109], v[158:161], v[174:177], 0
	v_mfma_f32_16x16x32_bf16 v[98:101], v[150:153], v[182:185], 0
	v_mfma_f32_16x16x32_bf16 v[90:93], v[158:161], v[182:185], 0
	v_mfma_f32_16x16x32_bf16 v[82:85], v[150:153], v[190:193], 0
	v_mfma_f32_16x16x32_bf16 v[74:77], v[158:161], v[190:193], 0
	v_mfma_f32_16x16x32_bf16 v[130:133], v[154:157], v[170:173], v[130:133]
	v_mfma_f32_16x16x32_bf16 v[122:125], v[162:165], v[170:173], v[122:125]
	v_mfma_f32_16x16x32_bf16 v[114:117], v[154:157], v[178:181], v[114:117]
	v_mfma_f32_16x16x32_bf16 v[106:109], v[162:165], v[178:181], v[106:109]
	v_mfma_f32_16x16x32_bf16 v[98:101], v[154:157], v[186:189], v[98:101]
	v_mfma_f32_16x16x32_bf16 v[90:93], v[162:165], v[186:189], v[90:93]
	v_mfma_f32_16x16x32_bf16 v[82:85], v[154:157], v[194:197], v[82:85]
	v_mfma_f32_16x16x32_bf16 v[74:77], v[162:165], v[194:197], v[74:77]
	s_setprio 0
	s_setprio 1
	v_mfma_f32_16x16x32_bf16 v[126:129], v[134:137], v[166:169], 0
	v_mfma_f32_16x16x32_bf16 v[118:121], v[142:145], v[166:169], 0
	v_mfma_f32_16x16x32_bf16 v[110:113], v[134:137], v[174:177], 0
	v_mfma_f32_16x16x32_bf16 v[102:105], v[142:145], v[174:177], 0
	v_mfma_f32_16x16x32_bf16 v[94:97], v[134:137], v[182:185], 0
	v_mfma_f32_16x16x32_bf16 v[86:89], v[142:145], v[182:185], 0
	v_mfma_f32_16x16x32_bf16 v[78:81], v[134:137], v[190:193], 0
	v_mfma_f32_16x16x32_bf16 v[70:73], v[142:145], v[190:193], 0
	v_mfma_f32_16x16x32_bf16 v[126:129], v[138:141], v[170:173], v[126:129]
	v_mfma_f32_16x16x32_bf16 v[118:121], v[146:149], v[170:173], v[118:121]
	v_mfma_f32_16x16x32_bf16 v[110:113], v[138:141], v[178:181], v[110:113]
	v_mfma_f32_16x16x32_bf16 v[102:105], v[146:149], v[178:181], v[102:105]
	v_mfma_f32_16x16x32_bf16 v[94:97], v[138:141], v[186:189], v[94:97]
	v_mfma_f32_16x16x32_bf16 v[86:89], v[146:149], v[186:189], v[86:89]
	v_mfma_f32_16x16x32_bf16 v[78:81], v[138:141], v[194:197], v[78:81]
	v_mfma_f32_16x16x32_bf16 v[70:73], v[146:149], v[194:197], v[70:73]
	s_setprio 0
	s_barrier
	s_add_i32 s73, s76, s47
	s_and_b64 s[4:5], s[38:39], s[4:5]
	v_lshl_add_u64 v[210:211], s[42:43], 0, v[202:203]
	s_mov_b32 m0, s73
	ds_read_b128 v[190:193], v247 offset:16384
	ds_read_b128 v[194:197], v247 offset:17408
	ds_read_b128 v[182:185], v247 offset:18432
	ds_read_b128 v[186:189], v247 offset:19456
	ds_read_b128 v[174:177], v247 offset:20480
	ds_read_b128 v[178:181], v247 offset:21504
	ds_read_b128 v[166:169], v247 offset:22528
	ds_read_b128 v[170:173], v247 offset:23552
	s_xor_b64 s[4:5], s[4:5], -1
	global_load_lds_dwordx4 v[210:211], off
	s_add_i32 m0, s73, 0x2000
	v_lshl_add_u64 v[212:213], s[42:43], 0, v[204:205]
	s_add_u32 s42, s42, s16
	s_addc_u32 s43, s43, s17
	s_add_i32 s72, s72, s47
	global_load_lds_dwordx4 v[212:213], off
	v_lshl_add_u64 v[216:217], s[42:43], 0, v[202:203]
	s_mov_b32 m0, s72
	v_lshl_add_u64 v[218:219], s[42:43], 0, v[204:205]
	global_load_lds_dwordx4 v[216:217], off
	s_add_i32 m0, s72, 0x2000
	s_mov_b64 s[42:43], -1
	global_load_lds_dwordx4 v[218:219], off
	s_and_b64 vcc, exec, s[4:5]
	v_lshl_add_u64 v[214:215], s[40:41], 0, v[34:35]
	s_cbranch_vccz .Lgp_751
	s_mov_b32 m0, s48
	s_mov_b64 s[42:43], 0
	global_load_lds_dwordx4 v[214:215], off

.Lgp_753:
	v_lshl_add_u64 v[220:221], s[40:41], 0, v[220:221]
	s_mov_b32 m0, s49
	s_nop 0
	global_load_lds_dwordx4 v[220:221], off
	s_cmp_lg_u32 s65, 1
	s_cbranch_scc1 .Lgp_skipw
	s_waitcnt vmcnt(8)
.Lgp_skipw:
	s_waitcnt lgkmcnt(0)
	s_barrier
	s_setprio 1
	s_waitcnt lgkmcnt(0)
	v_mfma_f32_16x16x32_bf16 v[66:69], v[150:153], v[190:193], 0
	v_mfma_f32_16x16x32_bf16 v[58:61], v[158:161], v[190:193], 0
	v_mfma_f32_16x16x32_bf16 v[50:53], v[150:153], v[182:185], 0
	v_mfma_f32_16x16x32_bf16 v[42:45], v[158:161], v[182:185], 0
	v_mfma_f32_16x16x32_bf16 v[30:33], v[150:153], v[174:177], 0
	v_mfma_f32_16x16x32_bf16 v[22:25], v[158:161], v[174:177], 0
	v_mfma_f32_16x16x32_bf16 v[14:17], v[150:153], v[166:169], 0
	v_mfma_f32_16x16x32_bf16 v[6:9], v[158:161], v[166:169], 0
	v_mfma_f32_16x16x32_bf16 v[66:69], v[154:157], v[194:197], v[66:69]
	v_mfma_f32_16x16x32_bf16 v[58:61], v[162:165], v[194:197], v[58:61]
	v_mfma_f32_16x16x32_bf16 v[50:53], v[154:157], v[186:189], v[50:53]
	v_mfma_f32_16x16x32_bf16 v[42:45], v[162:165], v[186:189], v[42:45]
	v_mfma_f32_16x16x32_bf16 v[30:33], v[154:157], v[178:181], v[30:33]
	v_mfma_f32_16x16x32_bf16 v[22:25], v[162:165], v[178:181], v[22:25]
	v_mfma_f32_16x16x32_bf16 v[14:17], v[154:157], v[170:173], v[14:17]
	v_mfma_f32_16x16x32_bf16 v[6:9], v[162:165], v[170:173], v[6:9]
	s_setprio 0
	s_setprio 1
	v_mfma_f32_16x16x32_bf16 v[62:65], v[134:137], v[190:193], 0
	v_mfma_f32_16x16x32_bf16 v[54:57], v[142:145], v[190:193], 0
	v_mfma_f32_16x16x32_bf16 v[46:49], v[134:137], v[182:185], 0
	v_mfma_f32_16x16x32_bf16 v[38:41], v[142:145], v[182:185], 0
	v_mfma_f32_16x16x32_bf16 v[26:29], v[134:137], v[174:177], 0
	v_mfma_f32_16x16x32_bf16 v[18:21], v[142:145], v[174:177], 0
	v_mfma_f32_16x16x32_bf16 v[10:13], v[134:137], v[166:169], 0
	v_mfma_f32_16x16x32_bf16 v[2:5], v[142:145], v[166:169], 0
	v_mfma_f32_16x16x32_bf16 v[62:65], v[138:141], v[194:197], v[62:65]
	v_mfma_f32_16x16x32_bf16 v[54:57], v[146:149], v[194:197], v[54:57]
	v_mfma_f32_16x16x32_bf16 v[46:49], v[138:141], v[186:189], v[46:49]
	v_mfma_f32_16x16x32_bf16 v[38:41], v[146:149], v[186:189], v[38:41]
	v_mfma_f32_16x16x32_bf16 v[26:29], v[138:141], v[178:181], v[26:29]
	v_mfma_f32_16x16x32_bf16 v[18:21], v[146:149], v[178:181], v[18:21]
	v_mfma_f32_16x16x32_bf16 v[10:13], v[138:141], v[170:173], v[10:13]
	v_mfma_f32_16x16x32_bf16 v[2:5], v[146:149], v[170:173], v[2:5]
	s_setprio 0
	s_barrier
	v_add_u32_e32 v0, 0, v244
	v_add_u32_e32 v134, 0x18000, v0
	v_add_u32_e32 v0, 0x1c000, v0
	ds_read_b128 v[150:153], v134
	ds_read_b128 v[154:157], v134 offset:1024
	ds_read_b128 v[158:161], v134 offset:2048
	ds_read_b128 v[162:165], v134 offset:3072
	ds_read_b128 v[134:137], v0
	ds_read_b128 v[138:141], v0 offset:1024
	ds_read_b128 v[142:145], v0 offset:2048
	ds_read_b128 v[146:149], v0 offset:3072
	ds_read_b128 v[190:193], v247 offset:32768
	ds_read_b128 v[194:197], v247 offset:33792
	ds_read_b128 v[182:185], v247 offset:34816
	ds_read_b128 v[186:189], v247 offset:35840
	ds_read_b128 v[174:177], v247 offset:36864
	ds_read_b128 v[178:181], v247 offset:37888
	ds_read_b128 v[166:169], v247 offset:38912
	ds_read_b128 v[170:173], v247 offset:39936
	s_mov_b64 s[42:43], -1
	s_and_b64 vcc, exec, s[4:5]
	s_cbranch_vccz .Lgp_755
	s_mov_b32 m0, s50
	v_lshl_add_u64 v[220:221], s[40:41], 0, v[36:37]
	global_load_lds_dwordx4 v[220:221], off
	s_mov_b64 s[42:43], 0

.Lgp_748:
	v_lshl_add_u64 v[210:211], s[40:41], 0, v[210:211]
	s_mov_b32 m0, s58
	v_lshl_add_u64 v[210:211], v[210:211], 0, s[94:95]
	global_load_lds_dwordx4 v[210:211], off
	s_waitcnt vmcnt(8)
	s_waitcnt lgkmcnt(0)
	s_add_i32 s71, s71, 2
	s_barrier
	s_setprio 1
	s_waitcnt lgkmcnt(0)
	v_mfma_f32_16x16x32_bf16 v[66:69], v[150:153], v[190:193], v[66:69]
	v_mfma_f32_16x16x32_bf16 v[58:61], v[158:161], v[190:193], v[58:61]
	v_mfma_f32_16x16x32_bf16 v[50:53], v[150:153], v[182:185], v[50:53]
	v_mfma_f32_16x16x32_bf16 v[42:45], v[158:161], v[182:185], v[42:45]
	v_mfma_f32_16x16x32_bf16 v[30:33], v[150:153], v[174:177], v[30:33]
	v_mfma_f32_16x16x32_bf16 v[22:25], v[158:161], v[174:177], v[22:25]
	v_mfma_f32_16x16x32_bf16 v[14:17], v[150:153], v[166:169], v[14:17]
	v_mfma_f32_16x16x32_bf16 v[6:9], v[158:161], v[166:169], v[6:9]
	v_mfma_f32_16x16x32_bf16 v[66:69], v[154:157], v[194:197], v[66:69]
	v_mfma_f32_16x16x32_bf16 v[58:61], v[162:165], v[194:197], v[58:61]
	v_mfma_f32_16x16x32_bf16 v[50:53], v[154:157], v[186:189], v[50:53]
	v_mfma_f32_16x16x32_bf16 v[42:45], v[162:165], v[186:189], v[42:45]
	v_mfma_f32_16x16x32_bf16 v[30:33], v[154:157], v[178:181], v[30:33]
	v_mfma_f32_16x16x32_bf16 v[22:25], v[162:165], v[178:181], v[22:25]
	v_mfma_f32_16x16x32_bf16 v[14:17], v[154:157], v[170:173], v[14:17]
	v_mfma_f32_16x16x32_bf16 v[6:9], v[162:165], v[170:173], v[6:9]
	s_setprio 0
	s_setprio 1
	v_mfma_f32_16x16x32_bf16 v[62:65], v[134:137], v[190:193], v[62:65]
	v_mfma_f32_16x16x32_bf16 v[54:57], v[142:145], v[190:193], v[54:57]
	v_mfma_f32_16x16x32_bf16 v[46:49], v[134:137], v[182:185], v[46:49]
	v_mfma_f32_16x16x32_bf16 v[38:41], v[142:145], v[182:185], v[38:41]
	v_mfma_f32_16x16x32_bf16 v[26:29], v[134:137], v[174:177], v[26:29]
	v_mfma_f32_16x16x32_bf16 v[18:21], v[142:145], v[174:177], v[18:21]
	v_mfma_f32_16x16x32_bf16 v[10:13], v[134:137], v[166:169], v[10:13]
	v_mfma_f32_16x16x32_bf16 v[2:5], v[142:145], v[166:169], v[2:5]
	v_mfma_f32_16x16x32_bf16 v[62:65], v[138:141], v[194:197], v[62:65]
	v_mfma_f32_16x16x32_bf16 v[54:57], v[146:149], v[194:197], v[54:57]
	v_mfma_f32_16x16x32_bf16 v[46:49], v[138:141], v[186:189], v[46:49]
	v_mfma_f32_16x16x32_bf16 v[38:41], v[146:149], v[186:189], v[38:41]
	v_mfma_f32_16x16x32_bf16 v[26:29], v[138:141], v[178:181], v[26:29]
	v_mfma_f32_16x16x32_bf16 v[18:21], v[146:149], v[178:181], v[18:21]
	v_mfma_f32_16x16x32_bf16 v[10:13], v[138:141], v[170:173], v[10:13]
	v_mfma_f32_16x16x32_bf16 v[2:5], v[146:149], v[170:173], v[2:5]
	s_setprio 0
	s_barrier
	s_add_u32 s69, s69, 0x100
	s_addc_u32 s70, s70, 0
	s_add_u32 s8, s8, 0x100
	s_addc_u32 s9, s9, 0
	s_cmp_ge_i32 s71, s15
	s_cbranch_scc1 .LBB0_761
	s_branch .LBB0_749

.LBB0_768:
	v_mul_f32_e32 v0, 0xbfb8aa3b, v130
	v_exp_f32_e32 v0, v0
	v_mul_f32_e32 v35, 0xbfb8aa3b, v131
	v_exp_f32_e32 v37, v35
	v_lshl_add_u32 v36, s66, 8, v242
	v_add_f32_e32 v0, 1.0, v0
	v_rcp_f32_e32 v134, v0
	v_add_f32_e32 v0, 1.0, v37
	v_rcp_f32_e32 v135, v0
	v_ashrrev_i32_e32 v37, 31, v36
	v_mul_f32_e32 v0, 0xbfb8aa3b, v132
	v_lshlrev_b64 v[136:137], 10, v[36:37]
	v_exp_f32_e32 v0, v0
	v_mul_f32_e32 v37, 0xbfb8aa3b, v133
	v_exp_f32_e32 v37, v37
	v_pk_mul_f32 v[130:131], v[130:131], v[134:135]
	v_add_f32_e32 v0, 1.0, v0
	v_pk_mul_f32 v[126:127], v[126:127], v[130:131]
	v_rcp_f32_e32 v130, v0
	v_add_f32_e32 v0, 1.0, v37
	v_rcp_f32_e32 v131, v0
	v_mul_f32_e32 v0, 0xbfb8aa3b, v122
	v_exp_f32_e32 v0, v0
	v_mul_f32_e32 v37, 0xbfb8aa3b, v123
	v_exp_f32_e32 v37, v37
	v_pk_mul_f32 v[130:131], v[132:133], v[130:131]
	v_add_f32_e32 v0, 1.0, v0
	v_rcp_f32_e32 v132, v0
	v_add_f32_e32 v0, 1.0, v37
	v_mul_f32_e32 v37, 0xbfb8aa3b, v124
	v_exp_f32_e32 v37, v37
	v_mul_f32_e32 v133, 0xbfb8aa3b, v125
	v_exp_f32_e32 v135, v133
	v_rcp_f32_e32 v133, v0
	v_add_f32_e32 v0, 1.0, v37
	v_rcp_f32_e32 v134, v0
	v_add_f32_e32 v0, 1.0, v135
	v_rcp_f32_e32 v135, v0
	v_mul_f32_e32 v0, 0xbfb8aa3b, v114
	v_exp_f32_e32 v0, v0
	v_mul_f32_e32 v37, 0xbfb8aa3b, v115
	v_lshl_add_u32 v34, s67, 7, v246
	v_pk_mul_f32 v[122:123], v[122:123], v[132:133]
	v_exp_f32_e32 v37, v37
	v_ashrrev_i32_e32 v35, 31, v34
	v_pk_mul_f32 v[122:123], v[118:119], v[122:123]
	v_pk_mul_f32 v[118:119], v[124:125], v[134:135]
	v_lshl_add_u64 v[136:137], s[20:21], 0, v[136:137]
	v_pk_mul_f32 v[128:129], v[128:129], v[130:131]
	v_pk_mul_f32 v[124:125], v[120:121], v[118:119]
	v_lshlrev_b64 v[118:119], 1, v[34:35]
	v_lshl_add_u64 v[34:35], v[136:137], 0, v[118:119]
	v_cvt_pk_bf16_f32 v120, v126, v127
	v_cvt_pk_bf16_f32 v121, v128, v129
	v_cvt_pk_bf16_f32 v122, v122, v123
	v_cvt_pk_bf16_f32 v123, v124, v125
	v_add_f32_e32 v0, 1.0, v0
	global_store_dwordx4 v[34:35], v[120:123], off
	s_mov_b32 s4, 0x20000
	s_nop 0
	v_rcp_f32_e32 v122, v0
	v_add_f32_e32 v0, 1.0, v37
	v_rcp_f32_e32 v123, v0
	v_mul_f32_e32 v0, 0xbfb8aa3b, v116
	v_exp_f32_e32 v0, v0
	v_mul_f32_e32 v37, 0xbfb8aa3b, v117
	v_exp_f32_e32 v37, v37
	v_pk_mul_f32 v[114:115], v[114:115], v[122:123]
	v_add_f32_e32 v0, 1.0, v0
	v_pk_mul_f32 v[110:111], v[110:111], v[114:115]
	v_rcp_f32_e32 v114, v0
	v_add_f32_e32 v0, 1.0, v37
	v_rcp_f32_e32 v115, v0
	v_mul_f32_e32 v0, 0xbfb8aa3b, v106
	v_exp_f32_e32 v0, v0
	v_mul_f32_e32 v37, 0xbfb8aa3b, v107
	v_exp_f32_e32 v37, v37
	v_pk_mul_f32 v[114:115], v[116:117], v[114:115]
	v_add_f32_e32 v0, 1.0, v0
	v_rcp_f32_e32 v116, v0
	v_add_f32_e32 v0, 1.0, v37
	v_mul_f32_e32 v37, 0xbfb8aa3b, v108
	v_exp_f32_e32 v37, v37
	v_mul_f32_e32 v117, 0xbfb8aa3b, v109
	v_exp_f32_e32 v123, v117
	v_rcp_f32_e32 v117, v0
	v_add_f32_e32 v0, 1.0, v37
	v_rcp_f32_e32 v122, v0
	v_add_f32_e32 v0, 1.0, v123
	v_rcp_f32_e32 v123, v0
	v_mul_f32_e32 v0, 0xbfb8aa3b, v98
	v_or_b32_e32 v120, 16, v36
	v_exp_f32_e32 v0, v0
	v_mul_f32_e32 v37, 0xbfb8aa3b, v99
	v_ashrrev_i32_e32 v121, 31, v120
	v_pk_mul_f32 v[106:107], v[106:107], v[116:117]
	v_exp_f32_e32 v37, v37
	v_lshlrev_b64 v[120:121], 10, v[120:121]
	v_pk_mul_f32 v[106:107], v[102:103], v[106:107]
	v_pk_mul_f32 v[102:103], v[108:109], v[122:123]
	v_lshl_add_u64 v[120:121], s[20:21], 0, v[120:121]
	v_pk_mul_f32 v[112:113], v[112:113], v[114:115]
	v_pk_mul_f32 v[108:109], v[104:105], v[102:103]
	v_lshl_add_u64 v[114:115], v[120:121], 0, v[118:119]
	v_cvt_pk_bf16_f32 v102, v110, v111
	v_cvt_pk_bf16_f32 v103, v112, v113
	v_cvt_pk_bf16_f32 v104, v106, v107
	v_cvt_pk_bf16_f32 v105, v108, v109
	v_add_f32_e32 v0, 1.0, v0
	global_store_dwordx4 v[114:115], v[102:105], off
	s_nop 1
	v_rcp_f32_e32 v104, v0
	v_add_f32_e32 v0, 1.0, v37
	v_rcp_f32_e32 v105, v0
	v_mul_f32_e32 v0, 0xbfb8aa3b, v100
	v_exp_f32_e32 v0, v0
	v_mul_f32_e32 v37, 0xbfb8aa3b, v101
	v_exp_f32_e32 v37, v37
	v_pk_mul_f32 v[98:99], v[98:99], v[104:105]
	v_add_f32_e32 v0, 1.0, v0
	v_pk_mul_f32 v[94:95], v[94:95], v[98:99]
	v_rcp_f32_e32 v98, v0
	v_add_f32_e32 v0, 1.0, v37
	v_rcp_f32_e32 v99, v0
	v_mul_f32_e32 v0, 0xbfb8aa3b, v90
	v_exp_f32_e32 v0, v0
	v_mul_f32_e32 v37, 0xbfb8aa3b, v91
	v_exp_f32_e32 v37, v37
	v_pk_mul_f32 v[98:99], v[100:101], v[98:99]
	v_add_f32_e32 v0, 1.0, v0
	v_rcp_f32_e32 v100, v0
	v_add_f32_e32 v0, 1.0, v37
	v_mul_f32_e32 v37, 0xbfb8aa3b, v92
	v_exp_f32_e32 v37, v37
	v_mul_f32_e32 v101, 0xbfb8aa3b, v93
	v_exp_f32_e32 v105, v101
	v_rcp_f32_e32 v101, v0
	v_add_f32_e32 v0, 1.0, v37
	v_rcp_f32_e32 v104, v0
	v_add_f32_e32 v0, 1.0, v105
	v_rcp_f32_e32 v105, v0
	v_mul_f32_e32 v0, 0xbfb8aa3b, v82
	v_or_b32_e32 v102, 32, v36
	v_exp_f32_e32 v0, v0
	v_mul_f32_e32 v37, 0xbfb8aa3b, v83
	v_ashrrev_i32_e32 v103, 31, v102
	v_pk_mul_f32 v[90:91], v[90:91], v[100:101]
	v_exp_f32_e32 v37, v37
	v_lshlrev_b64 v[102:103], 10, v[102:103]
	v_pk_mul_f32 v[90:91], v[86:87], v[90:91]
	v_pk_mul_f32 v[86:87], v[92:93], v[104:105]
	v_lshl_add_u64 v[102:103], s[20:21], 0, v[102:103]
	v_pk_mul_f32 v[96:97], v[96:97], v[98:99]
	v_pk_mul_f32 v[92:93], v[88:89], v[86:87]
	v_lshl_add_u64 v[98:99], v[102:103], 0, v[118:119]
	v_cvt_pk_bf16_f32 v86, v94, v95
	v_cvt_pk_bf16_f32 v87, v96, v97
	v_cvt_pk_bf16_f32 v88, v90, v91
	v_cvt_pk_bf16_f32 v89, v92, v93
	v_add_f32_e32 v0, 1.0, v0
	global_store_dwordx4 v[98:99], v[86:89], off
	v_or_b32_e32 v36, 48, v36
	s_nop 0
	v_rcp_f32_e32 v86, v0
	v_add_f32_e32 v0, 1.0, v37
	v_rcp_f32_e32 v87, v0
	v_mul_f32_e32 v0, 0xbfb8aa3b, v84
	v_exp_f32_e32 v0, v0
	v_ashrrev_i32_e32 v37, 31, v36
	v_pk_mul_f32 v[82:83], v[82:83], v[86:87]
	v_mul_f32_e32 v86, 0xbfb8aa3b, v85
	v_exp_f32_e32 v86, v86
	v_add_f32_e32 v0, 1.0, v0
	v_pk_mul_f32 v[78:79], v[78:79], v[82:83]
	v_rcp_f32_e32 v82, v0
	v_add_f32_e32 v0, 1.0, v86
	v_rcp_f32_e32 v83, v0
	v_mul_f32_e32 v0, 0xbfb8aa3b, v74
	v_exp_f32_e32 v0, v0
	v_mul_f32_e32 v86, 0xbfb8aa3b, v75
	v_exp_f32_e32 v86, v86
	v_pk_mul_f32 v[82:83], v[84:85], v[82:83]
	v_add_f32_e32 v0, 1.0, v0
	v_mul_f32_e32 v85, 0xbfb8aa3b, v76
	v_rcp_f32_e32 v84, v0
	v_add_f32_e32 v0, 1.0, v86
	v_exp_f32_e32 v86, v85
	v_mul_f32_e32 v85, 0xbfb8aa3b, v77
	v_exp_f32_e32 v87, v85
	v_rcp_f32_e32 v85, v0
	v_add_f32_e32 v0, 1.0, v86
	v_rcp_f32_e32 v86, v0
	v_add_f32_e32 v0, 1.0, v87
	v_rcp_f32_e32 v87, v0
	v_pk_mul_f32 v[74:75], v[74:75], v[84:85]
	v_mul_f32_e32 v0, 0xbfb8aa3b, v66
	v_pk_mul_f32 v[74:75], v[70:71], v[74:75]
	v_pk_mul_f32 v[70:71], v[76:77], v[86:87]
	v_exp_f32_e32 v0, v0
	v_pk_mul_f32 v[76:77], v[72:73], v[70:71]
	v_mul_f32_e32 v71, 0xbfb8aa3b, v67
	v_exp_f32_e32 v72, v71
	v_add_f32_e32 v0, 1.0, v0
	v_cvt_pk_bf16_f32 v70, v78, v79
	v_rcp_f32_e32 v78, v0
	v_add_f32_e32 v0, 1.0, v72
	v_rcp_f32_e32 v79, v0
	v_lshlrev_b64 v[36:37], 10, v[36:37]
	v_lshl_add_u64 v[36:37], s[20:21], 0, v[36:37]
	v_pk_mul_f32 v[80:81], v[80:81], v[82:83]
	v_lshl_add_u64 v[36:37], v[36:37], 0, v[118:119]
	v_cvt_pk_bf16_f32 v71, v80, v81
	v_cvt_pk_bf16_f32 v72, v74, v75
	v_cvt_pk_bf16_f32 v73, v76, v77
	v_mul_f32_e32 v0, 0xbfb8aa3b, v68
	global_store_dwordx4 v[36:37], v[70:73], off
	v_pk_mul_f32 v[36:37], v[66:67], v[78:79]
	v_exp_f32_e32 v0, v0
	v_mul_f32_e32 v66, 0xbfb8aa3b, v69
	v_exp_f32_e32 v66, v66
	v_pk_mul_f32 v[36:37], v[62:63], v[36:37]
	v_add_f32_e32 v0, 1.0, v0
	v_rcp_f32_e32 v62, v0
	v_add_f32_e32 v0, 1.0, v66
	v_rcp_f32_e32 v63, v0
	v_mul_f32_e32 v0, 0xbfb8aa3b, v58
	v_exp_f32_e32 v0, v0
	v_mul_f32_e32 v66, 0xbfb8aa3b, v59
	v_exp_f32_e32 v67, v66
	v_pk_mul_f32 v[62:63], v[68:69], v[62:63]
	v_add_f32_e32 v0, 1.0, v0
	v_rcp_f32_e32 v66, v0
	v_add_f32_e32 v0, 1.0, v67
	v_mul_f32_e32 v67, 0xbfb8aa3b, v60
	v_exp_f32_e32 v68, v67
	v_mul_f32_e32 v67, 0xbfb8aa3b, v61
	v_exp_f32_e32 v69, v67
	v_rcp_f32_e32 v67, v0
	v_add_f32_e32 v0, 1.0, v68
	v_rcp_f32_e32 v68, v0
	v_add_f32_e32 v0, 1.0, v69
	v_rcp_f32_e32 v69, v0
	v_pk_mul_f32 v[58:59], v[58:59], v[66:67]
	v_mul_f32_e32 v0, 0xbfb8aa3b, v50
	v_pk_mul_f32 v[58:59], v[54:55], v[58:59]
	v_pk_mul_f32 v[54:55], v[60:61], v[68:69]
	v_exp_f32_e32 v0, v0
	v_pk_mul_f32 v[60:61], v[56:57], v[54:55]
	v_cvt_pk_bf16_f32 v54, v36, v37
	v_mul_f32_e32 v36, 0xbfb8aa3b, v51
	v_exp_f32_e32 v37, v36
	v_add_f32_e32 v0, 1.0, v0
	v_rcp_f32_e32 v36, v0
	v_cvt_pk_bf16_f32 v56, v58, v59
	v_add_f32_e32 v0, 1.0, v37
	v_rcp_f32_e32 v37, v0
	v_mul_f32_e32 v0, 0xbfb8aa3b, v52
	v_exp_f32_e32 v0, v0
	v_add_co_u32_e32 v58, vcc, s4, v34
	v_pk_mul_f32 v[36:37], v[50:51], v[36:37]
	v_mul_f32_e32 v50, 0xbfb8aa3b, v53
	v_exp_f32_e32 v50, v50
	v_add_f32_e32 v0, 1.0, v0
	v_pk_mul_f32 v[36:37], v[46:47], v[36:37]
	v_rcp_f32_e32 v46, v0
	v_add_f32_e32 v0, 1.0, v50
	v_rcp_f32_e32 v47, v0
	v_mul_f32_e32 v0, 0xbfb8aa3b, v42
	v_exp_f32_e32 v0, v0
	v_mul_f32_e32 v50, 0xbfb8aa3b, v43
	v_exp_f32_e32 v51, v50
	v_pk_mul_f32 v[46:47], v[52:53], v[46:47]
	v_add_f32_e32 v0, 1.0, v0
	v_rcp_f32_e32 v50, v0
	v_add_f32_e32 v0, 1.0, v51
	v_mul_f32_e32 v51, 0xbfb8aa3b, v44
	v_exp_f32_e32 v52, v51
	v_mul_f32_e32 v51, 0xbfb8aa3b, v45
	v_exp_f32_e32 v53, v51
	v_rcp_f32_e32 v51, v0
	v_add_f32_e32 v0, 1.0, v52
	v_rcp_f32_e32 v52, v0
	v_add_f32_e32 v0, 1.0, v53
	v_rcp_f32_e32 v53, v0
	v_pk_mul_f32 v[42:43], v[42:43], v[50:51]
	v_mul_f32_e32 v0, 0xbfb8aa3b, v30
	v_pk_mul_f32 v[38:39], v[38:39], v[42:43]
	v_pk_mul_f32 v[42:43], v[44:45], v[52:53]
	v_cvt_pk_bf16_f32 v38, v38, v39
	v_exp_f32_e32 v0, v0
	v_mul_f32_e32 v39, 0xbfb8aa3b, v31
	v_pk_mul_f32 v[40:41], v[40:41], v[42:43]
	v_exp_f32_e32 v42, v39
	v_addc_co_u32_e32 v59, vcc, 0, v35, vcc
	v_add_f32_e32 v0, 1.0, v0
	s_mov_b32 s4, 0x24000
	v_pk_mul_f32 v[46:47], v[48:49], v[46:47]
	v_cvt_pk_bf16_f32 v39, v40, v41
	v_rcp_f32_e32 v40, v0
	v_add_f32_e32 v0, 1.0, v42
	v_add_co_u32_e32 v42, vcc, s4, v34
	v_cvt_pk_bf16_f32 v36, v36, v37
	v_cvt_pk_bf16_f32 v37, v46, v47
	v_rcp_f32_e32 v41, v0
	v_addc_co_u32_e32 v43, vcc, 0, v35, vcc
	v_mul_f32_e32 v0, 0xbfb8aa3b, v32
	global_store_dwordx4 v[42:43], v[36:39], off
	v_exp_f32_e32 v0, v0
	v_pk_mul_f32 v[30:31], v[30:31], v[40:41]
	v_mul_f32_e32 v36, 0xbfb8aa3b, v33
	v_exp_f32_e32 v36, v36
	v_add_f32_e32 v0, 1.0, v0
	v_pk_mul_f32 v[26:27], v[26:27], v[30:31]
	v_rcp_f32_e32 v30, v0
	v_add_f32_e32 v0, 1.0, v36
	v_rcp_f32_e32 v31, v0
	v_mul_f32_e32 v0, 0xbfb8aa3b, v22
	v_exp_f32_e32 v0, v0
	v_mul_f32_e32 v36, 0xbfb8aa3b, v23
	v_exp_f32_e32 v36, v36
	v_pk_mul_f32 v[30:31], v[32:33], v[30:31]
	v_add_f32_e32 v0, 1.0, v0
	v_mul_f32_e32 v33, 0xbfb8aa3b, v24
	v_rcp_f32_e32 v32, v0
	v_add_f32_e32 v0, 1.0, v36
	v_exp_f32_e32 v36, v33
	v_mul_f32_e32 v33, 0xbfb8aa3b, v25
	v_exp_f32_e32 v37, v33
	v_rcp_f32_e32 v33, v0
	v_add_f32_e32 v0, 1.0, v36
	v_rcp_f32_e32 v36, v0
	v_add_f32_e32 v0, 1.0, v37
	v_rcp_f32_e32 v37, v0
	v_pk_mul_f32 v[22:23], v[22:23], v[32:33]
	v_mul_f32_e32 v0, 0xbfb8aa3b, v14
	v_pk_mul_f32 v[22:23], v[18:19], v[22:23]
	v_pk_mul_f32 v[18:19], v[24:25], v[36:37]
	v_exp_f32_e32 v0, v0
	v_pk_mul_f32 v[24:25], v[20:21], v[18:19]
	v_mul_f32_e32 v21, 0xbfb8aa3b, v15
	v_cvt_pk_bf16_f32 v20, v22, v23
	v_exp_f32_e32 v23, v21
	v_add_f32_e32 v0, 1.0, v0
	s_mov_b32 s4, 0x28000
	v_pk_mul_f32 v[28:29], v[28:29], v[30:31]
	v_cvt_pk_bf16_f32 v21, v24, v25
	v_rcp_f32_e32 v22, v0
	v_add_f32_e32 v0, 1.0, v23
	v_add_co_u32_e32 v24, vcc, s4, v34
	v_cvt_pk_bf16_f32 v18, v26, v27
	v_cvt_pk_bf16_f32 v19, v28, v29
	v_rcp_f32_e32 v23, v0
	v_addc_co_u32_e32 v25, vcc, 0, v35, vcc
	v_mul_f32_e32 v0, 0xbfb8aa3b, v16
	global_store_dwordx4 v[24:25], v[18:21], off
	v_exp_f32_e32 v0, v0
	v_pk_mul_f32 v[14:15], v[14:15], v[22:23]
	v_mul_f32_e32 v18, 0xbfb8aa3b, v17
	v_exp_f32_e32 v18, v18
	v_add_f32_e32 v0, 1.0, v0
	v_pk_mul_f32 v[10:11], v[10:11], v[14:15]
	v_rcp_f32_e32 v14, v0
	v_add_f32_e32 v0, 1.0, v18
	v_rcp_f32_e32 v15, v0
	v_mul_f32_e32 v0, 0xbfb8aa3b, v6
	v_exp_f32_e32 v0, v0
	v_mul_f32_e32 v18, 0xbfb8aa3b, v7
	v_exp_f32_e32 v18, v18
	v_pk_mul_f32 v[14:15], v[16:17], v[14:15]
	v_add_f32_e32 v0, 1.0, v0
	v_mul_f32_e32 v17, 0xbfb8aa3b, v8
	v_rcp_f32_e32 v16, v0
	v_add_f32_e32 v0, 1.0, v18
	v_exp_f32_e32 v18, v17
	v_mul_f32_e32 v17, 0xbfb8aa3b, v9
	v_exp_f32_e32 v19, v17
	v_rcp_f32_e32 v17, v0
	v_add_f32_e32 v0, 1.0, v18
	v_rcp_f32_e32 v18, v0
	v_add_f32_e32 v0, 1.0, v19
	v_rcp_f32_e32 v19, v0
	v_pk_mul_f32 v[6:7], v[6:7], v[16:17]
	v_pk_mul_f32 v[62:63], v[64:65], v[62:63]
	v_pk_mul_f32 v[6:7], v[2:3], v[6:7]
	v_pk_mul_f32 v[2:3], v[8:9], v[18:19]
	v_pk_mul_f32 v[12:13], v[12:13], v[14:15]
	v_pk_mul_f32 v[8:9], v[4:5], v[2:3]
	v_cvt_pk_bf16_f32 v4, v6, v7
	v_add_co_u32_e32 v6, vcc, 0x2c000, v34
	v_cvt_pk_bf16_f32 v55, v62, v63
	s_nop 0
	v_addc_co_u32_e32 v7, vcc, 0, v35, vcc
	v_cvt_pk_bf16_f32 v57, v60, v61
	v_cvt_pk_bf16_f32 v2, v10, v11
	v_cvt_pk_bf16_f32 v3, v12, v13
	v_cvt_pk_bf16_f32 v5, v8, v9
	s_and_b64 vcc, exec, s[6:7]
	s_mov_b64 s[4:5], -1
	global_store_dwordx4 v[58:59], v[54:57], off
	global_store_dwordx4 v[6:7], v[2:5], off
	s_waitcnt vmcnt(8)
	s_cbranch_vccnz .LBB0_741
	ds_read_b128 v[34:37], v253
	s_andn2_b64 vcc, exec, s[18:19]
	s_cbranch_vccnz .LBB0_740
	s_barrier
	s_branch .LBB0_740
